# v13a: v8 + scan state waves at s_setprio 1 only while stepping chunks (0 during the triangular solve)
# speedup vs baseline: 1.0085x; 1.0041x over previous
.LBB0_1725:
	s_setprio 0
	s_cmp_eq_u32 s82, 0
	s_cbranch_scc1 .Lx14_w0
	s_waitcnt vmcnt(8)
	s_branch .Lx14_wj

.LBB0_1728:
	s_or_b64 exec, exec, s[68:69]
	s_waitcnt lgkmcnt(0)
	s_and_saveexec_b64 s[68:69], s[4:5]
	s_add_i32 s0, s71, 1
	v_mov_b32_e32 v18, s61
	v_mov_b32_e32 v19, s0
	ds_write_b32 v18, v19
	s_setprio 1
	s_or_b64 exec, exec, s[68:69]
	s_lshl_b32 s68, s71, 2
	s_mov_b32 s69, 0
	s_branch .LBB0_1732
